# GLA chunk: prefetch waits + 40 register copies moved from the chunk end into the state-update MFMA section (behind its LDS reads)
# speedup vs baseline: 1.0057x; 1.0006x over previous
.LBB0_468:
	s_add_i32 s91, s91, 64
	s_sub_i32 s89, s89, 64
	s_add_i32 s92, s92, 1
	s_cmpk_eq_i32 s91, 0x900
	s_cbranch_scc1 .LBB0_466

.Lgo_pos:
	v_lshl_add_u32 v251, v215, 9, v218
	v_add_u32_e32 v252, s0, v251
	v_add_u32_e32 v253, s1, v251
	v_add_u32_e32 v216, s1, v252
	ds_read_b128 v[30:33], v97 offset:9216
	ds_read_b128 v[40:43], v97 offset:9280
	ds_read_b128 v[44:47], v97 offset:11520
	ds_read_b128 v[52:55], v97 offset:2304
	ds_read_b128 v[60:63], v97 offset:11584
	ds_read_b128 v[64:67], v97 offset:2368
	ds_read_b128 v[72:75], v98 offset:9216
	ds_read_b128 v[142:145], v98
	ds_read_b128 v[146:149], v98 offset:9280
	ds_read_b128 v[150:153], v98 offset:64
	ds_read_b128 v[154:157], v99 offset:9216
	ds_read_b128 v[158:161], v99
	ds_read_b128 v[162:165], v99 offset:9280
	ds_read_b128 v[166:169], v99 offset:64
	ds_read_b128 v[48:51], v97 offset:64
	ds_read_b128 v[56:59], v97
	s_waitcnt lgkmcnt(0)
	v_mfma_f32_16x16x32_bf16 v[56:59], v[30:33], v[56:59], 0
	v_mfma_f32_16x16x32_bf16 v[48:51], v[40:43], v[48:51], v[56:59]
	s_nop 7
	v_cndmask_b32_e64 v35, v51, 0, s[40:41]
	v_cndmask_b32_e64 v141, v50, 0, s[62:63]
	v_cndmask_b32_e64 v170, v49, 0, s[72:73]
	v_cndmask_b32_e64 v171, v48, 0, s[2:3]
	v_mfma_f32_16x16x32_bf16 v[48:51], v[30:33], v[52:55], 0
	v_mfma_f32_16x16x32_bf16 v[56:59], v[40:43], v[64:67], v[48:51]
	v_mfma_f32_16x16x32_bf16 v[48:51], v[30:33], v[142:145], 0
	v_mfma_f32_16x16x32_bf16 v[30:33], v[30:33], v[158:161], 0
	v_mfma_f32_16x16x32_bf16 v[48:51], v[40:43], v[150:153], v[48:51]
	v_mfma_f32_16x16x32_bf16 v[40:43], v[40:43], v[166:169], v[30:33]
	v_mfma_f32_16x16x32_bf16 v[30:33], v[44:47], v[52:55], 0
	v_mfma_f32_16x16x32_bf16 v[30:33], v[60:63], v[64:67], v[30:33]
	v_cvt_pk_bf16_f32 v64, v26, v27
	v_cvt_pk_bf16_f32 v65, v28, v29
	v_cvt_pk_bf16_f32 v66, v36, v37
	v_cvt_pk_bf16_f32 v67, v38, v39
	s_nop 3
	v_cndmask_b32_e64 v172, v33, 0, s[40:41]
	v_cndmask_b32_e64 v173, v32, 0, s[62:63]
	v_cndmask_b32_e64 v174, v31, 0, s[72:73]
	v_cndmask_b32_e64 v175, v30, 0, s[2:3]
	v_mfma_f32_16x16x32_bf16 v[30:33], v[44:47], v[142:145], 0
	v_mfma_f32_16x16x32_bf16 v[68:71], v[60:63], v[150:153], v[30:33]
	v_mfma_f32_16x16x32_bf16 v[30:33], v[44:47], v[158:161], 0
	v_mfma_f32_16x16x32_bf16 v[52:55], v[60:63], v[166:169], v[30:33]
	v_cvt_pk_bf16_f32 v60, v18, v19
	v_cvt_pk_bf16_f32 v61, v20, v21
	v_cvt_pk_bf16_f32 v62, v22, v23
	v_mfma_f32_16x16x32_bf16 v[30:33], v[72:75], v[142:145], 0
	v_cvt_pk_bf16_f32 v63, v24, v25
	v_mfma_f32_16x16x32_bf16 v[30:33], v[146:149], v[150:153], v[30:33]
	s_nop 7
	v_cndmask_b32_e64 v150, v33, 0, s[40:41]
	v_cndmask_b32_e64 v151, v32, 0, s[62:63]
	v_cndmask_b32_e64 v152, v31, 0, s[72:73]
	v_cndmask_b32_e64 v153, v30, 0, s[2:3]
	v_mfma_f32_16x16x32_bf16 v[30:33], v[72:75], v[158:161], 0
	v_mfma_f32_16x16x32_bf16 v[44:47], v[146:149], v[166:169], v[30:33]
	v_mfma_f32_16x16x32_bf16 v[30:33], v[154:157], v[158:161], 0
	v_mfma_f32_16x16x32_bf16 v[30:33], v[162:165], v[166:169], v[30:33]
	s_nop 7
	v_cndmask_b32_e64 v157, v30, 0, s[2:3]
	v_add_u32_e32 v30, 0x6800, v106
	ds_read2_b64 v[142:145], v30 offset0:128 offset1:132
	ds_read2_b64 v[72:75], v30 offset0:136 offset1:140
	v_cndmask_b32_e64 v154, v33, 0, s[40:41]
	v_cndmask_b32_e64 v155, v32, 0, s[62:63]
	v_cvt_pk_bf16_f32 v32, v171, v170
	v_cvt_pk_bf16_f32 v33, v141, v35
	v_mov_b32_e32 v35, v34
	ds_read2_b64 v[146:149], v101 offset1:4
	v_cndmask_b32_e64 v156, v31, 0, s[72:73]
	s_waitcnt lgkmcnt(2)
	v_mfma_f32_16x16x32_bf16 v[30:33], v[142:145], v[32:35], 0
	s_waitcnt lgkmcnt(0)
	v_mfma_f32_16x16x32_bf16 v[30:33], v[60:63], v[146:149], v[30:33]
	ds_read2_b64 v[146:149], v101 offset0:8 offset1:12
	s_waitcnt lgkmcnt(0)
	v_mfma_f32_16x16x32_bf16 v[30:33], v[64:67], v[146:149], v[30:33]
	s_nop 7
	v_mul_f32_e32 v30, 4.0, v30
	v_mul_f32_e32 v31, 4.0, v31
	v_mul_f32_e32 v32, 4.0, v32
	v_mul_f32_e32 v33, 4.0, v33
	v_med3_f32 v30, v30, s75, v238
	v_med3_f32 v31, v31, s75, v238
	v_med3_f32 v32, v32, s75, v238
	v_med3_f32 v33, v33, s75, v238
	v_cvt_pk_fp8_f32 v247, v30, v31
	s_nop 1
	v_cvt_pk_fp8_f32 v247, v32, v33 op_sel:[0,0,1]
	s_nop 1
	global_store_dword v251, v247, s[94:95]
	v_cvt_pk_bf16_f32 v30, v56, v57
	v_cvt_pk_bf16_f32 v31, v58, v59
	v_cvt_pk_bf16_f32 v32, v175, v174
	v_cvt_pk_bf16_f32 v33, v173, v172
	ds_read2_b64 v[56:59], v102 offset1:4
	s_nop 0
	v_mfma_f32_16x16x32_bf16 v[30:33], v[142:145], v[30:33], 0
	s_waitcnt lgkmcnt(0)
	v_mfma_f32_16x16x32_bf16 v[30:33], v[60:63], v[56:59], v[30:33]
	ds_read2_b64 v[56:59], v102 offset0:8 offset1:12
	s_waitcnt lgkmcnt(0)
	v_mfma_f32_16x16x32_bf16 v[30:33], v[64:67], v[56:59], v[30:33]
	s_nop 7
	v_mul_f32_e32 v30, 4.0, v30
	v_mul_f32_e32 v31, 4.0, v31
	v_mul_f32_e32 v32, 4.0, v32
	v_mul_f32_e32 v33, 4.0, v33
	v_med3_f32 v30, v30, s75, v238
	v_med3_f32 v31, v31, s75, v238
	v_med3_f32 v32, v32, s75, v238
	v_med3_f32 v33, v33, s75, v238
	v_cvt_pk_fp8_f32 v248, v30, v31
	s_nop 1
	v_cvt_pk_fp8_f32 v248, v32, v33 op_sel:[0,0,1]
	s_nop 1
	global_store_dword v252, v248, s[94:95]
	v_cvt_pk_bf16_f32 v30, v48, v49
	v_cvt_pk_bf16_f32 v31, v50, v51
	v_cvt_pk_bf16_f32 v32, v68, v69
	v_cvt_pk_bf16_f32 v33, v70, v71
	s_nop 1
	v_mfma_f32_16x16x32_bf16 v[48:51], v[142:145], v[30:33], 0
	v_cvt_pk_bf16_f32 v32, v153, v152
	v_cvt_pk_bf16_f32 v33, v151, v150
	s_nop 1
	v_mfma_f32_16x16x32_bf16 v[30:33], v[72:75], v[32:35], v[48:51]
	v_add_u32_e32 v35, v95, v105
	s_nop 1
	ds_read2_b64 v[48:51], v103 offset1:4
	s_waitcnt lgkmcnt(0)
	v_mfma_f32_16x16x32_bf16 v[30:33], v[60:63], v[48:51], v[30:33]
	ds_read2_b64 v[48:51], v103 offset0:8 offset1:12
	s_waitcnt lgkmcnt(0)
	v_mfma_f32_16x16x32_bf16 v[30:33], v[64:67], v[48:51], v[30:33]
	s_nop 7
	v_mul_f32_e32 v30, 4.0, v30
	v_mul_f32_e32 v31, 4.0, v31
	v_mul_f32_e32 v32, 4.0, v32
	v_mul_f32_e32 v33, 4.0, v33
	v_med3_f32 v30, v30, s75, v238
	v_med3_f32 v31, v31, s75, v238
	v_med3_f32 v32, v32, s75, v238
	v_med3_f32 v33, v33, s75, v238
	v_cvt_pk_fp8_f32 v249, v30, v31
	s_nop 1
	v_cvt_pk_fp8_f32 v249, v32, v33 op_sel:[0,0,1]
	s_nop 1
	global_store_dword v253, v249, s[94:95]
	v_cvt_pk_bf16_f32 v30, v40, v41
	v_cvt_pk_bf16_f32 v31, v42, v43
	v_cvt_pk_bf16_f32 v32, v52, v53
	v_cvt_pk_bf16_f32 v33, v54, v55
	v_cvt_pk_bf16_f32 v40, v44, v45
	v_cvt_pk_bf16_f32 v41, v46, v47
	v_mfma_f32_16x16x32_bf16 v[30:33], v[142:145], v[30:33], 0
	v_cvt_pk_bf16_f32 v42, v157, v156
	v_cvt_pk_bf16_f32 v43, v155, v154
	v_add_u32_e32 v44, v95, v100
	s_nop 0
	v_mfma_f32_16x16x32_bf16 v[30:33], v[72:75], v[40:43], v[30:33]
	ds_read2_b64 v[40:43], v104 offset1:4
	s_waitcnt lgkmcnt(0)
	v_mfma_f32_16x16x32_bf16 v[30:33], v[60:63], v[40:43], v[30:33]
	ds_read2_b64 v[40:43], v104 offset0:8 offset1:12
	s_waitcnt lgkmcnt(0)
	v_mfma_f32_16x16x32_bf16 v[30:33], v[64:67], v[40:43], v[30:33]
	s_nop 7
	v_mul_f32_e32 v30, 4.0, v30
	v_mul_f32_e32 v31, 4.0, v31
	v_mul_f32_e32 v32, 4.0, v32
	v_mul_f32_e32 v33, 4.0, v33
	v_med3_f32 v30, v30, s75, v238
	v_med3_f32 v31, v31, s75, v238
	v_med3_f32 v32, v32, s75, v238
	v_med3_f32 v33, v33, s75, v238
	v_cvt_pk_fp8_f32 v250, v30, v31
	s_nop 1
	v_cvt_pk_fp8_f32 v250, v32, v33 op_sel:[0,0,1]
	s_nop 1
	global_store_dword v216, v250, s[94:95]
	ds_read_b128 v[30:33], v114 offset:48128
	ds_read_b128 v[40:43], v44 offset:18432
	s_waitcnt lgkmcnt(1)
	v_pk_mul_f32 v[18:19], v[18:19], v[30:31]
	v_pk_mul_f32 v[20:21], v[20:21], v[32:33]
	ds_read_b128 v[30:33], v114 offset:48192
	s_waitcnt lgkmcnt(0)
	v_pk_mul_f32 v[22:23], v[22:23], v[30:31]
	v_pk_mul_f32 v[24:25], v[24:25], v[32:33]
	ds_read_b128 v[30:33], v114 offset:48256
	s_waitcnt lgkmcnt(0)
	v_pk_mul_f32 v[26:27], v[26:27], v[30:31]
	v_pk_mul_f32 v[28:29], v[28:29], v[32:33]
	ds_read_b128 v[30:33], v114 offset:48320
	s_waitcnt lgkmcnt(0)
	v_pk_mul_f32 v[30:31], v[36:37], v[30:31]
	v_pk_mul_f32 v[32:33], v[38:39], v[32:33]
	ds_read_b128 v[36:39], v35 offset:27648
	s_waitcnt vmcnt(38)
	v_mov_b32_e32 v115, v178
	v_mov_b32_e32 v116, v179
	v_mov_b32_e32 v117, v180
	v_mov_b32_e32 v118, v181
	v_mov_b32_e32 v119, v182
	v_mov_b32_e32 v120, v183
	s_waitcnt lgkmcnt(0)
	v_mfma_f32_16x16x32_bf16 v[18:21], v[40:43], v[36:39], v[18:21]
	ds_read_b128 v[40:43], v44 offset:20736
	s_waitcnt vmcnt(32)
	v_mov_b32_e32 v121, v184
	v_mov_b32_e32 v122, v185
	v_mov_b32_e32 v123, v186
	v_mov_b32_e32 v124, v187
	v_mov_b32_e32 v125, v188
	v_mov_b32_e32 v128, v189
	s_waitcnt lgkmcnt(0)
	v_mfma_f32_16x16x32_bf16 v[22:25], v[40:43], v[36:39], v[22:25]
	ds_read_b128 v[40:43], v44 offset:23040
	s_waitcnt vmcnt(26)
	v_mov_b32_e32 v129, v190
	v_mov_b32_e32 v130, v192
	v_mov_b32_e32 v131, v194
	v_mov_b32_e32 v132, v196
	v_mov_b32_e32 v133, v200
	v_mov_b32_e32 v134, v201
	s_waitcnt lgkmcnt(0)
	v_mfma_f32_16x16x32_bf16 v[26:29], v[40:43], v[36:39], v[26:29]
	ds_read_b128 v[40:43], v44 offset:25344
	s_waitcnt vmcnt(20)
	v_mov_b32_e32 v135, v202
	v_mov_b32_e32 v136, v203
	v_mov_b32_e32 v137, v206
	v_mov_b32_e32 v138, v207
	v_mov_b32_e32 v139, v208
	v_mov_b32_e32 v140, v209
	s_waitcnt lgkmcnt(0)
	v_mfma_f32_16x16x32_bf16 v[30:33], v[40:43], v[36:39], v[30:33]
	ds_read_b128 v[36:39], v35 offset:27712
	ds_read_b128 v[40:43], v44 offset:18496
	s_waitcnt vmcnt(16)
	v_mov_b32_e32 v2, v220
	v_mov_b32_e32 v1, v219
	v_mov_b32_e32 v4, v222
	v_mov_b32_e32 v3, v221
	s_waitcnt lgkmcnt(0)
	v_mfma_f32_16x16x32_bf16 v[18:21], v[40:43], v[36:39], v[18:21]
	ds_read_b128 v[40:43], v44 offset:20800
	s_waitcnt vmcnt(12)
	v_mov_b32_e32 v6, v224
	v_mov_b32_e32 v5, v223
	v_mov_b32_e32 v8, v226
	v_mov_b32_e32 v7, v225
	s_waitcnt lgkmcnt(0)
	v_mfma_f32_16x16x32_bf16 v[22:25], v[40:43], v[36:39], v[22:25]
	ds_read_b128 v[40:43], v44 offset:23104
	s_waitcnt vmcnt(8)
	v_mov_b32_e32 v10, v228
	v_mov_b32_e32 v9, v227
	v_mov_b32_e32 v12, v230
	v_mov_b32_e32 v11, v229
	s_waitcnt lgkmcnt(0)
	v_mfma_f32_16x16x32_bf16 v[26:29], v[40:43], v[36:39], v[26:29]
	ds_read_b128 v[40:43], v44 offset:25408
	s_waitcnt vmcnt(4)
	v_mov_b32_e32 v14, v232
	v_mov_b32_e32 v13, v231
	v_mov_b32_e32 v16, v246
	v_mov_b32_e32 v15, v233
	s_waitcnt lgkmcnt(0)
	v_mfma_f32_16x16x32_bf16 v[36:39], v[40:43], v[36:39], v[30:33]
	s_nop 2
	s_branch .LBB0_468
